# baseline (speedup 1.0000x reference)
.Lp1_fin:
	s_lshl_b64 s[0:1], s[20:21], 1
	s_add_u32 s0, s18, s0
	s_addc_u32 s1, s19, s1
	global_load_dwordx4 v[2:5], v[66:67], off
	global_load_dwordx4 v[6:9], v[68:69], off
	v_lshlrev_b32_e32 v10, 1, v79
	global_load_dwordx4 v[10:13], v10, s[0:1]
	v_lshlrev_b32_e32 v14, 1, v80
	global_load_dwordx4 v[14:17], v14, s[0:1]
	v_mov_b32_e32 v200, 0
	v_mov_b32_e32 v201, 0
	v_mov_b32_e32 v202, 0
	v_mov_b32_e32 v83, 0
	v_exp_f32_e32 v34, v34
	v_exp_f32_e32 v35, v35
	v_add_f32_e32 v200, v200, v34
	v_exp_f32_e32 v36, v36
	v_add_f32_e32 v201, v201, v35
	v_exp_f32_e32 v37, v37
	v_add_f32_e32 v202, v202, v36
	v_exp_f32_e32 v38, v38
	v_add_f32_e32 v83, v83, v37
	v_exp_f32_e32 v39, v39
	v_add_f32_e32 v200, v200, v38
	v_exp_f32_e32 v40, v40
	v_add_f32_e32 v201, v201, v39
	v_exp_f32_e32 v41, v41
	v_add_f32_e32 v202, v202, v40
	v_exp_f32_e32 v42, v42
	v_add_f32_e32 v83, v83, v41
	v_exp_f32_e32 v43, v43
	v_add_f32_e32 v200, v200, v42
	v_exp_f32_e32 v44, v44
	v_add_f32_e32 v201, v201, v43
	v_exp_f32_e32 v45, v45
	v_add_f32_e32 v202, v202, v44
	v_exp_f32_e32 v46, v46
	v_add_f32_e32 v83, v83, v45
	v_exp_f32_e32 v47, v47
	v_add_f32_e32 v200, v200, v46
	v_exp_f32_e32 v48, v48
	v_add_f32_e32 v201, v201, v47
	v_exp_f32_e32 v49, v49
	v_add_f32_e32 v202, v202, v48
	v_exp_f32_e32 v50, v50
	v_add_f32_e32 v83, v83, v49
	v_exp_f32_e32 v51, v51
	v_add_f32_e32 v200, v200, v50
	v_exp_f32_e32 v52, v52
	v_add_f32_e32 v201, v201, v51
	v_exp_f32_e32 v53, v53
	v_add_f32_e32 v202, v202, v52
	v_exp_f32_e32 v54, v54
	v_add_f32_e32 v83, v83, v53
	v_exp_f32_e32 v55, v55
	v_add_f32_e32 v200, v200, v54
	v_exp_f32_e32 v56, v56
	v_add_f32_e32 v201, v201, v55
	v_exp_f32_e32 v57, v57
	v_add_f32_e32 v202, v202, v56
	v_exp_f32_e32 v58, v58
	v_add_f32_e32 v83, v83, v57
	v_exp_f32_e32 v59, v59
	v_add_f32_e32 v200, v200, v58
	v_exp_f32_e32 v60, v60
	v_add_f32_e32 v201, v201, v59
	v_exp_f32_e32 v61, v61
	v_add_f32_e32 v202, v202, v60
	v_exp_f32_e32 v62, v62
	v_add_f32_e32 v83, v83, v61
	v_exp_f32_e32 v63, v63
	v_add_f32_e32 v200, v200, v62
	v_exp_f32_e32 v64, v64
	v_add_f32_e32 v201, v201, v63
	v_exp_f32_e32 v65, v65
	v_add_f32_e32 v202, v202, v64
	v_add_f32_e32 v83, v83, v65
	v_add_f32_e32 v200, v200, v201
	v_add_f32_e32 v202, v202, v83
	v_add_f32_e32 v200, v200, v202
	v_add_f32_e32 v82, v82, v200
	s_barrier
	v_mbcnt_lo_u32_b32 v21, -1, 0
	v_mbcnt_hi_u32_b32 v21, -1, v21
	v_and_b32_e32 v23, 64, v21
	v_xor_b32_e32 v22, 32, v21
	v_add_u32_e32 v24, 64, v23
	v_cmp_lt_i32_e32 vcc, v22, v24
	v_cndmask_b32_e32 v21, v21, v22, vcc
	v_lshlrev_b32_e32 v21, 2, v21
	ds_bpermute_b32 v22, v21, v81
	v_mov_b32_e32 v18, v82
	ds_bpermute_b32 v19, v21, v18
	v_max_f32_e32 v21, v81, v81
	s_mov_b32 s15, 0
	s_waitcnt lgkmcnt(1)
	v_max_f32_e32 v20, v22, v22
	v_max_f32_e32 v20, v21, v20
	v_sub_f32_e32 v22, v22, v20
	v_sub_f32_e32 v21, v81, v20
	v_exp_f32_e32 v22, v22
	v_exp_f32_e32 v21, v21
	s_lshl_b64 s[18:19], s[14:15], 18
	v_mov_b32_e32 v131, 0
	s_waitcnt lgkmcnt(0)
	v_mul_f32_e32 v19, v22, v19
	v_fmac_f32_e32 v19, v18, v21
	v_div_scale_f32 v18, s[10:11], v19, v19, 1.0
	s_movk_i32 s10, 0x60
	s_nop 0
	v_mad_u32_u24 v188, v73, s10, v74
	v_mad_u32_u24 v189, v75, s10, v74
	s_waitcnt vmcnt(3)
	ds_write_b128 v77, v[2:5]
	s_waitcnt vmcnt(2)
	ds_write_b128 v78, v[6:9]
	v_lshlrev_b32_e32 v2, 1, v188
	s_waitcnt vmcnt(1)
	ds_write_b128 v2, v[10:13]
	v_lshlrev_b32_e32 v2, 1, v189
	s_mul_i32 s10, s14, 0x1200
	s_waitcnt vmcnt(0)
	ds_write_b128 v2, v[14:17]
	s_add_i32 s10, s10, 0xa800
	v_lshrrev_b32_e32 v2, 2, v0
	v_and_or_b32 v3, v2, 3, v1
	s_movk_i32 s11, 0x48
	v_mov_b32_e32 v5, s10
	v_add_u32_e32 v4, s10, v76
	v_mad_u32_u24 v5, v3, s11, v5
	s_lshl_b64 s[10:11], s[12:13], 24
	s_and_b32 s13, s2, 15
	s_lshl_b32 s13, s13, 20
	v_and_b32_e32 v0, 3, v0
	s_or_b32 s10, s10, s13
	v_and_or_b32 v0, v2, 4, v0
	s_add_u32 s10, s10, s18
	v_lshlrev_b32_e32 v0, 3, v0
	v_mul_u32_u24_e32 v2, 0xc0, v3
	v_lshlrev_b32_e32 v3, 13, v72
	s_addc_u32 s11, s11, s19
	v_or_b32_e32 v185, v2, v0
	v_or_b32_e32 v2, v3, v164
	s_add_u32 s10, s4, s10
	v_lshlrev_b32_e32 v130, 2, v2
	s_addc_u32 s11, s5, s11
	v_lshl_add_u64 v[2:3], s[10:11], 0, v[130:131]
	s_mov_b64 s[18:19], 0x80
	v_lshl_add_u64 v[132:133], v[2:3], 0, s[18:19]
	v_or_b32_e32 v2, 0x36000, v130
	v_mov_b32_e32 v3, v131
	v_lshl_add_u64 v[134:135], s[10:11], 0, v[2:3]
	v_or_b32_e32 v2, 0x2000, v130
	v_lshl_add_u64 v[2:3], s[10:11], 0, v[2:3]
	v_lshl_add_u64 v[136:137], v[2:3], 0, s[18:19]
	v_or_b32_e32 v2, 0x34000, v130
	v_mov_b32_e32 v3, v131
	v_rcp_f32_e32 v21, v18
	v_lshl_add_u64 v[138:139], s[10:11], 0, v[2:3]
	v_or_b32_e32 v2, 0x4000, v130
	v_lshl_add_u64 v[2:3], s[10:11], 0, v[2:3]
	v_lshl_add_u64 v[140:141], v[2:3], 0, s[18:19]
	v_or_b32_e32 v2, 0x32000, v130
	v_mov_b32_e32 v3, v131
	v_lshl_add_u64 v[142:143], s[10:11], 0, v[2:3]
	v_or_b32_e32 v2, 0x6000, v130
	v_fma_f32 v22, -v18, v21, 1.0
	v_lshl_add_u64 v[2:3], s[10:11], 0, v[2:3]
	v_fmac_f32_e32 v21, v22, v21
	v_div_scale_f32 v22, vcc, 1.0, v19, 1.0
	v_lshl_add_u64 v[144:145], v[2:3], 0, s[18:19]
	v_or_b32_e32 v2, 0x30000, v130
	v_mov_b32_e32 v3, v131
	v_mul_f32_e32 v24, v22, v21
	v_lshl_add_u64 v[146:147], s[10:11], 0, v[2:3]
	v_or_b32_e32 v2, 0x10000, v130
	v_fma_f32 v25, -v18, v24, v22
	v_lshl_add_u64 v[2:3], s[10:11], 0, v[2:3]
	v_fmac_f32_e32 v24, v25, v21
	v_lshl_add_u64 v[148:149], v[2:3], 0, s[18:19]
	v_or_b32_e32 v2, 0x26000, v130
	v_mov_b32_e32 v3, v131
	v_fma_f32 v18, -v18, v24, v22
	v_lshl_add_u64 v[150:151], s[10:11], 0, v[2:3]
	v_or_b32_e32 v2, 0x12000, v130
	v_div_fmas_f32 v18, v18, v21, v24
	v_lshlrev_b32_e32 v184, 2, v72
	v_lshl_add_u64 v[2:3], s[10:11], 0, v[2:3]
	v_div_fixup_f32 v18, v18, v19, 1.0
	v_or_b32_e32 v19, v184, v23
	v_lshl_add_u64 v[152:153], v[2:3], 0, s[18:19]
	v_or_b32_e32 v2, 0x24000, v130
	v_mov_b32_e32 v3, v131
	v_lshlrev_b32_e32 v19, 2, v19
	v_lshl_add_u64 v[154:155], s[10:11], 0, v[2:3]
	v_or_b32_e32 v2, 0x14000, v130
	ds_bpermute_b32 v33, v19, v20 offset:36
	ds_bpermute_b32 v32, v19, v20 offset:40
	ds_bpermute_b32 v35, v19, v20 offset:44
	ds_bpermute_b32 v34, v19, v20 offset:64
	ds_bpermute_b32 v37, v19, v20 offset:68
	ds_bpermute_b32 v36, v19, v20 offset:72
	ds_bpermute_b32 v39, v19, v20 offset:76
	ds_bpermute_b32 v38, v19, v20 offset:96
	ds_bpermute_b32 v41, v19, v20 offset:100
	ds_bpermute_b32 v40, v19, v20 offset:104
	ds_bpermute_b32 v43, v19, v20 offset:108
	v_lshl_add_u64 v[2:3], s[10:11], 0, v[2:3]
	ds_bpermute_b32 v46, v19, v20 offset:32
	ds_bpermute_b32 v47, v19, v20 offset:12
	ds_bpermute_b32 v42, v19, v20 offset:8
	ds_bpermute_b32 v45, v19, v20 offset:4
	ds_bpermute_b32 v44, v19, v20
	ds_bpermute_b32 v183, v19, v18
	ds_bpermute_b32 v182, v19, v18 offset:4
	ds_bpermute_b32 v181, v19, v18 offset:8
	ds_bpermute_b32 v180, v19, v18 offset:12
	ds_bpermute_b32 v179, v19, v18 offset:32
	ds_bpermute_b32 v178, v19, v18 offset:36
	ds_bpermute_b32 v177, v19, v18 offset:40
	ds_bpermute_b32 v176, v19, v18 offset:44
	ds_bpermute_b32 v175, v19, v18 offset:64
	ds_bpermute_b32 v174, v19, v18 offset:68
	ds_bpermute_b32 v173, v19, v18 offset:72
	ds_bpermute_b32 v172, v19, v18 offset:76
	ds_bpermute_b32 v171, v19, v18 offset:96
	ds_bpermute_b32 v170, v19, v18 offset:100
	ds_bpermute_b32 v169, v19, v18 offset:104
	ds_bpermute_b32 v168, v19, v18 offset:108
	v_lshl_add_u64 v[156:157], v[2:3], 0, s[18:19]
	v_or_b32_e32 v2, 0x22000, v130
	v_mov_b32_e32 v3, v131
	v_lshl_add_u64 v[158:159], s[10:11], 0, v[2:3]
	v_or_b32_e32 v2, 0x16000, v130
	v_lshl_add_u64 v[2:3], s[10:11], 0, v[2:3]
	v_lshl_add_u64 v[160:161], v[2:3], 0, s[18:19]
	v_or_b32_e32 v2, 0x20000, v130
	v_mov_b32_e32 v3, v131
	v_add_u32_e32 v187, v4, v1
	v_lshl_add_u64 v[162:163], s[10:11], 0, v[2:3]
	s_mov_b64 s[42:43], s[10:11]
	s_mov_b64 s[10:11], 0
	s_movk_i32 s13, 0x3000
	s_waitcnt lgkmcnt(14)
	v_xor_b32_e32 v63, 0x80000000, v43
	v_xor_b32_e32 v62, 0x80000000, v40
	v_xor_b32_e32 v61, 0x80000000, v41
	v_xor_b32_e32 v60, 0x80000000, v38
	v_xor_b32_e32 v59, 0x80000000, v39
	v_xor_b32_e32 v58, 0x80000000, v36
	v_xor_b32_e32 v57, 0x80000000, v37
	v_xor_b32_e32 v56, 0x80000000, v34
	v_xor_b32_e32 v55, 0x80000000, v35
	v_xor_b32_e32 v54, 0x80000000, v32
	v_xor_b32_e32 v53, 0x80000000, v33
	v_add_u32_e32 v186, v5, v0
	v_xor_b32_e32 v52, 0x80000000, v46
	v_xor_b32_e32 v51, 0x80000000, v47
	v_xor_b32_e32 v50, 0x80000000, v42
	v_xor_b32_e32 v49, 0x80000000, v45
	v_xor_b32_e32 v48, 0x80000000, v44
	v_mov_b32_e32 v0, v131
	v_mov_b32_e32 v1, v131
	v_mov_b32_e32 v2, v131
	v_mov_b32_e32 v4, v131
	v_mov_b32_e32 v5, v131
	v_mov_b32_e32 v6, v131
	v_mov_b32_e32 v7, v131
	v_mov_b32_e32 v8, v131
	v_mov_b32_e32 v9, v131
	v_mov_b32_e32 v10, v131
	v_mov_b32_e32 v11, v131
	v_mov_b32_e32 v12, v131
	v_mov_b32_e32 v13, v131
	v_mov_b32_e32 v14, v131
	v_mov_b32_e32 v15, v131
	v_mov_b32_e32 v16, v131
	v_mov_b32_e32 v17, v131
	v_mov_b32_e32 v18, v131
	v_mov_b32_e32 v19, v131
	v_mov_b32_e32 v20, v131
	v_mov_b32_e32 v21, v131
	v_mov_b32_e32 v22, v131
	v_mov_b32_e32 v23, v131
	v_mov_b32_e32 v24, v131
	v_mov_b32_e32 v25, v131
	v_mov_b32_e32 v26, v131
	v_mov_b32_e32 v27, v131
	v_mov_b32_e32 v28, v131
	v_mov_b32_e32 v29, v131
	v_mov_b32_e32 v30, v131
	v_mov_b32_e32 v31, v131
	v_add_u32_e32 v131, 0x800, v187
	v_or_b32_e32 v132, 0x80, v130
	v_or_b32_e32 v136, 0x2080, v130
	v_or_b32_e32 v140, 0x4080, v130
	v_or_b32_e32 v144, 0x6080, v130
	v_or_b32_e32 v148, 0x10080, v130
	v_or_b32_e32 v152, 0x12080, v130
	v_or_b32_e32 v156, 0x14080, v130
	v_or_b32_e32 v160, 0x16080, v130
	v_or_b32_e32 v162, 0x20000, v130
	v_or_b32_e32 v158, 0x22000, v130
	v_or_b32_e32 v154, 0x24000, v130
	v_or_b32_e32 v150, 0x26000, v130
	v_or_b32_e32 v146, 0x30000, v130
	v_or_b32_e32 v142, 0x32000, v130
	v_or_b32_e32 v138, 0x34000, v130
	v_or_b32_e32 v134, 0x36000, v130
	s_add_u32 s8, s8, 0x2000
	s_addc_u32 s9, s9, 0
	s_add_u32 s0, s0, 0x2000
	s_addc_u32 s1, s1, 0
	v_add_u32_e32 v204, 0x1000, v128
	s_waitcnt lgkmcnt(0)
	v_mov_b32_e32 v228, v183
	v_mov_b32_e32 v229, v182
	v_mov_b32_e32 v230, v181
	v_mov_b32_e32 v231, v180
	v_mov_b32_e32 v232, v179
	v_mov_b32_e32 v233, v178
	v_mov_b32_e32 v234, v177
	v_mov_b32_e32 v235, v176
	v_mov_b32_e32 v236, v175
	v_mov_b32_e32 v237, v174
	v_mov_b32_e32 v238, v173
	v_mov_b32_e32 v239, v172
	v_mov_b32_e32 v240, v171
	v_mov_b32_e32 v241, v170
	v_mov_b32_e32 v242, v169
	v_mov_b32_e32 v243, v168
	s_barrier
.LBB4_11:
	s_and_b32 s14, s15, 1
	global_load_dwordx4 v[112:115], v128, s[8:9]
	global_load_dwordx4 v[116:119], v204, s[8:9]
	global_load_dwordx4 v[120:123], v128, s[0:1]
	global_load_dwordx4 v[124:127], v204, s[0:1]
	s_add_i32 s15, s15, 1
	s_mul_i32 s18, s14, 0x2400
	v_add_u32_e32 v202, s18, v167
	ds_read_b128 v[80:83], v202
	ds_read_b128 v[190:193], v202 offset:32
	ds_read_b128 v[194:197], v202 offset:4608
	ds_read_b128 v[198:201], v202 offset:4640
	s_waitcnt lgkmcnt(3)
	v_mfma_f32_32x32x16_f16 v[64:79], v[108:111], v[80:83], v[48:63]
	s_waitcnt lgkmcnt(1)
	v_mfma_f32_32x32x16_f16 v[80:95], v[108:111], v[194:197], v[48:63]
	v_mfma_f32_32x32x16_f16 v[64:79], v[104:107], v[190:193], v[64:79]
	ds_read_b128 v[190:193], v202 offset:64
	ds_read_b128 v[194:197], v202 offset:96
	s_waitcnt lgkmcnt(2)
	v_mfma_f32_32x32x16_f16 v[80:95], v[104:107], v[198:201], v[80:95]
	s_waitcnt lgkmcnt(1)
	v_mfma_f32_32x32x16_f16 v[64:79], v[100:103], v[190:193], v[64:79]
	ds_read_b128 v[190:193], v202 offset:4672
	ds_read_b128 v[198:201], v202 offset:4704
	s_waitcnt lgkmcnt(1)
	v_mfma_f32_32x32x16_f16 v[80:95], v[100:103], v[190:193], v[80:95]
	v_mfma_f32_32x32x16_f16 v[64:79], v[96:99], v[194:197], v[64:79]
	s_waitcnt lgkmcnt(0)
	v_mfma_f32_32x32x16_f16 v[80:95], v[96:99], v[198:201], v[80:95]
	s_setprio 2
	s_nop 8
	v_exp_f32_e32 v64, v64
	v_exp_f32_e32 v65, v65
	v_exp_f32_e32 v66, v66
	v_pk_mul_f32 v[222:223], v[64:65], v[228:229]
	v_exp_f32_e32 v67, v67
	v_cvt_pk_f16_f32 v206, v64, v65
	v_exp_f32_e32 v68, v68
	v_pk_mul_f32 v[224:225], v[66:67], v[230:231]
	v_exp_f32_e32 v69, v69
	v_cvt_pk_f16_f32 v207, v66, v67
	global_store_dword v132, v222, s[42:43] offset:-128
	global_store_dword v136, v223, s[42:43] offset:-128
	v_exp_f32_e32 v70, v70
	v_pk_mul_f32 v[226:227], v[68:69], v[232:233]
	v_exp_f32_e32 v71, v71
	v_cvt_pk_f16_f32 v208, v68, v69
	global_store_dword v140, v224, s[42:43] offset:-128
	global_store_dword v144, v225, s[42:43] offset:-128
	v_exp_f32_e32 v80, v80
	v_pk_mul_f32 v[222:223], v[70:71], v[234:235]
	v_exp_f32_e32 v81, v81
	v_cvt_pk_f16_f32 v209, v70, v71
	global_store_dword v148, v226, s[42:43] offset:-128
	global_store_dword v152, v227, s[42:43] offset:-128
	v_exp_f32_e32 v82, v82
	v_pk_mul_f32 v[224:225], v[80:81], v[228:229]
	v_exp_f32_e32 v83, v83
	v_cvt_pk_f16_f32 v214, v80, v81
	global_store_dword v156, v222, s[42:43] offset:-128
	global_store_dword v160, v223, s[42:43] offset:-128
	v_exp_f32_e32 v84, v84
	v_pk_mul_f32 v[226:227], v[82:83], v[230:231]
	v_exp_f32_e32 v85, v85
	v_cvt_pk_f16_f32 v215, v82, v83
	global_store_dword v132, v224, s[42:43]
	global_store_dword v136, v225, s[42:43]
	v_exp_f32_e32 v86, v86
	v_pk_mul_f32 v[222:223], v[84:85], v[232:233]
	v_exp_f32_e32 v87, v87
	v_cvt_pk_f16_f32 v216, v84, v85
	global_store_dword v140, v226, s[42:43]
	global_store_dword v144, v227, s[42:43]
	v_exp_f32_e32 v72, v72
	v_pk_mul_f32 v[224:225], v[86:87], v[234:235]
	v_exp_f32_e32 v73, v73
	v_cvt_pk_f16_f32 v217, v86, v87
	global_store_dword v148, v222, s[42:43]
	global_store_dword v152, v223, s[42:43]
	ds_write2_b64 v187, v[206:207], v[208:209] offset0:0 offset1:2
	ds_write2_b64 v131, v[214:215], v[216:217] offset0:32 offset1:34
	v_exp_f32_e32 v74, v74
	v_pk_mul_f32 v[226:227], v[72:73], v[236:237]
	v_exp_f32_e32 v75, v75
	v_cvt_pk_f16_f32 v210, v72, v73
	global_store_dword v156, v224, s[42:43]
	global_store_dword v160, v225, s[42:43]
	v_exp_f32_e32 v76, v76
	v_pk_mul_f32 v[222:223], v[74:75], v[238:239]
	v_exp_f32_e32 v77, v77
	v_cvt_pk_f16_f32 v211, v74, v75
	global_store_dword v162, v226, s[42:43]
	global_store_dword v158, v227, s[42:43]
	v_exp_f32_e32 v78, v78
	v_pk_mul_f32 v[224:225], v[76:77], v[240:241]
	v_exp_f32_e32 v79, v79
	v_cvt_pk_f16_f32 v212, v76, v77
	global_store_dword v154, v222, s[42:43]
	global_store_dword v150, v223, s[42:43]
	v_exp_f32_e32 v88, v88
	v_pk_mul_f32 v[226:227], v[78:79], v[242:243]
	v_exp_f32_e32 v89, v89
	v_cvt_pk_f16_f32 v213, v78, v79
	global_store_dword v146, v224, s[42:43]
	global_store_dword v142, v225, s[42:43]
	v_exp_f32_e32 v90, v90
	v_pk_mul_f32 v[222:223], v[88:89], v[236:237]
	v_exp_f32_e32 v91, v91
	v_cvt_pk_f16_f32 v218, v88, v89
	global_store_dword v138, v226, s[42:43]
	global_store_dword v134, v227, s[42:43]
	v_exp_f32_e32 v92, v92
	v_pk_mul_f32 v[224:225], v[90:91], v[238:239]
	v_exp_f32_e32 v93, v93
	v_cvt_pk_f16_f32 v219, v90, v91
	global_store_dword v162, v222, s[42:43] offset:128
	global_store_dword v158, v223, s[42:43] offset:128
	v_exp_f32_e32 v94, v94
	v_pk_mul_f32 v[226:227], v[92:93], v[240:241]
	v_exp_f32_e32 v95, v95
	v_cvt_pk_f16_f32 v220, v92, v93
	global_store_dword v154, v224, s[42:43] offset:128
	global_store_dword v150, v225, s[42:43] offset:128
	v_pk_mul_f32 v[222:223], v[94:95], v[242:243]
	v_cvt_pk_f16_f32 v221, v94, v95
	global_store_dword v146, v226, s[42:43] offset:128
	global_store_dword v142, v227, s[42:43] offset:128
	ds_write2_b64 v187, v[210:211], v[212:213] offset0:4 offset1:6
	ds_write2_b64 v131, v[218:219], v[220:221] offset0:36 offset1:38
	global_store_dword v138, v222, s[42:43] offset:128
	global_store_dword v134, v223, s[42:43] offset:128
	s_setprio 0
	ds_read_b64_tr_b16 v[64:65], v186
	ds_read_b64_tr_b16 v[66:67], v186 offset:288
	s_mul_i32 s18, s14, 0x3000
	v_or_b32_e32 v80, s18, v185
	ds_read_b64_tr_b16 v[68:69], v80
	ds_read_b64_tr_b16 v[70:71], v80 offset:768
	ds_read_b64_tr_b16 v[74:75], v80 offset:832
	ds_read_b64_tr_b16 v[72:73], v80 offset:64
	ds_read_b64_tr_b16 v[76:77], v186 offset:1152
	ds_read_b64_tr_b16 v[78:79], v186 offset:1440
	s_waitcnt lgkmcnt(4)
	v_mfma_f32_32x32x16_f16 v[0:15], v[64:67], v[68:71], v[0:15]
	s_waitcnt lgkmcnt(2)
	v_mfma_f32_32x32x16_f16 v[16:31], v[64:67], v[72:75], v[16:31]
	ds_read_b64_tr_b16 v[64:65], v80 offset:3072
	ds_read_b64_tr_b16 v[66:67], v80 offset:3840
	ds_read_b64_tr_b16 v[70:71], v80 offset:3904
	ds_read_b64_tr_b16 v[68:69], v80 offset:3136
	s_waitcnt lgkmcnt(2)
	v_mfma_f32_32x32x16_f16 v[0:15], v[76:79], v[64:67], v[0:15]
	s_waitcnt lgkmcnt(0)
	v_mfma_f32_32x32x16_f16 v[16:31], v[76:79], v[68:71], v[16:31]
	ds_read_b64_tr_b16 v[64:65], v186 offset:2304
	ds_read_b64_tr_b16 v[66:67], v186 offset:2592
	ds_read_b64_tr_b16 v[68:69], v80 offset:6144
	ds_read_b64_tr_b16 v[70:71], v80 offset:6912
	ds_read_b64_tr_b16 v[74:75], v80 offset:6976
	ds_read_b64_tr_b16 v[72:73], v80 offset:6208
	ds_read_b64_tr_b16 v[76:77], v186 offset:3456
	ds_read_b64_tr_b16 v[78:79], v186 offset:3744
	s_waitcnt lgkmcnt(4)
	v_mfma_f32_32x32x16_f16 v[0:15], v[64:67], v[68:71], v[0:15]
	s_waitcnt lgkmcnt(2)
	v_mfma_f32_32x32x16_f16 v[16:31], v[64:67], v[72:75], v[16:31]
	ds_read_b64_tr_b16 v[64:65], v80 offset:9216
	ds_read_b64_tr_b16 v[66:67], v80 offset:9984
	ds_read_b64_tr_b16 v[70:71], v80 offset:10048
	ds_read_b64_tr_b16 v[68:69], v80 offset:9280
	s_waitcnt lgkmcnt(2)
	v_mfma_f32_32x32x16_f16 v[0:15], v[76:79], v[64:67], v[0:15]
	s_waitcnt lgkmcnt(0)
	v_mfma_f32_32x32x16_f16 v[16:31], v[76:79], v[68:71], v[16:31]
	s_xor_b32 s14, s14, 1
	s_mul_i32 s18, s14, 0x3000
	s_mulk_i32 s14, 0x2400
	s_addk_i32 s14, 0x6000
	s_add_u32 s10, s10, 0x100
	s_addc_u32 s11, s11, 0
	s_add_u32 s42, s42, 0x100
	s_addc_u32 s43, s43, 0
	s_add_u32 s8, s8, 0x2000
	s_addc_u32 s9, s9, 0
	s_add_u32 s0, s0, 0x2000
	s_addc_u32 s1, s1, 0
	v_lshl_add_u32 v67, v166, 1, s14
	s_cmpk_eq_i32 s10, 0x1f00
	v_lshl_add_u32 v64, v189, 1, s18
	v_lshl_add_u32 v65, v188, 1, s18
	v_lshl_add_u32 v66, v165, 1, s14
	s_waitcnt vmcnt(35)
	ds_write_b128 v67, v[112:115]
	s_waitcnt vmcnt(34)
	ds_write_b128 v66, v[116:119]
	s_waitcnt vmcnt(33)
	ds_write_b128 v65, v[120:123]
	s_waitcnt vmcnt(32)
	ds_write_b128 v64, v[124:127]
	s_waitcnt lgkmcnt(0)
	s_barrier
	s_cbranch_scc0 .LBB4_11
	s_lshl_b64 s[0:1], s[16:17], 13
	s_add_u32 s0, s4, s0
	s_addc_u32 s1, s5, s1
	v_xor_b32_e32 v52, 0x80000000, v34
	v_xor_b32_e32 v51, 0x80000000, v35
	v_xor_b32_e32 v50, 0x80000000, v32
	v_xor_b32_e32 v49, 0x80000000, v33
	ds_read_b128 v[32:35], v167 offset:9216
	v_xor_b32_e32 v59, 0x80000000, v43
	v_xor_b32_e32 v58, 0x80000000, v40
	v_xor_b32_e32 v57, 0x80000000, v41
	v_xor_b32_e32 v56, 0x80000000, v38
	v_xor_b32_e32 v55, 0x80000000, v39
	v_xor_b32_e32 v54, 0x80000000, v36
	v_xor_b32_e32 v53, 0x80000000, v37
	v_xor_b32_e32 v48, 0x80000000, v46
	v_xor_b32_e32 v47, 0x80000000, v47
	v_xor_b32_e32 v46, 0x80000000, v42
	v_xor_b32_e32 v45, 0x80000000, v45
	v_xor_b32_e32 v44, 0x80000000, v44
	ds_read_b128 v[36:39], v167 offset:9248
	s_add_u32 s0, s0, 0x1f00
	s_waitcnt lgkmcnt(1)
	v_mfma_f32_32x32x16_f16 v[60:75], v[108:111], v[32:35], v[44:59]
	ds_read_b128 v[32:35], v167 offset:13824
	ds_read_b128 v[40:43], v167 offset:13856
	s_addc_u32 s1, s1, 0
	s_waitcnt lgkmcnt(1)
	v_mfma_f32_32x32x16_f16 v[44:59], v[108:111], v[32:35], v[44:59]
	v_mfma_f32_32x32x16_f16 v[60:75], v[104:107], v[36:39], v[60:75]
	ds_read_b128 v[32:35], v167 offset:9280
	ds_read_b128 v[36:39], v167 offset:9312
	s_waitcnt lgkmcnt(2)
	v_mfma_f32_32x32x16_f16 v[44:59], v[104:107], v[40:43], v[44:59]
	s_waitcnt lgkmcnt(1)
	v_mfma_f32_32x32x16_f16 v[60:75], v[100:103], v[32:35], v[60:75]
	ds_read_b128 v[32:35], v167 offset:13888
	ds_read_b128 v[40:43], v167 offset:13920
	s_waitcnt lgkmcnt(1)
	v_mfma_f32_32x32x16_f16 v[44:59], v[100:103], v[32:35], v[44:59]
	v_mfma_f32_32x32x16_f16 v[60:75], v[96:99], v[36:39], v[60:75]
	s_waitcnt lgkmcnt(0)
	v_mfma_f32_32x32x16_f16 v[44:59], v[96:99], v[40:43], v[44:59]
	s_setprio 2
	s_nop 8
	v_exp_f32_e32 v32, v60
	s_nop 0
	v_exp_f32_e32 v34, v44
	v_exp_f32_e32 v35, v61
	v_or_b32_e32 v37, 0x2000, v130
	v_mul_f32_e32 v33, v32, v183
	v_mul_f32_e32 v36, v34, v183
	global_store_dword v130, v33, s[0:1]
	global_store_dword v130, v36, s[0:1] offset:128
	v_exp_f32_e32 v36, v45
	v_mul_f32_e32 v33, v35, v182
	global_store_dword v37, v33, s[0:1]
	v_exp_f32_e32 v33, v62
	v_mul_f32_e32 v38, v36, v182
	global_store_dword v37, v38, s[0:1] offset:128
	v_exp_f32_e32 v37, v46
	v_mul_f32_e32 v38, v33, v181
	v_or_b32_e32 v39, 0x4000, v130
	global_store_dword v39, v38, s[0:1]
	v_exp_f32_e32 v38, v63
	v_mul_f32_e32 v40, v37, v181
	global_store_dword v39, v40, s[0:1] offset:128
	v_exp_f32_e32 v39, v47
	v_mul_f32_e32 v40, v38, v180
	v_cvt_pk_f16_f32 v33, v33, v38
	v_exp_f32_e32 v38, v64
	v_or_b32_e32 v41, 0x6000, v130
	global_store_dword v41, v40, s[0:1]
	v_mul_f32_e32 v40, v39, v180
	global_store_dword v41, v40, s[0:1] offset:128
	v_cvt_pk_f16_f32 v32, v32, v35
	v_cvt_pk_f16_f32 v35, v37, v39
	v_cvt_pk_f16_f32 v34, v34, v36
	v_exp_f32_e32 v40, v48
	v_mul_f32_e32 v36, v38, v179
	v_or_b32_e32 v37, 0x10000, v130
	global_store_dword v37, v36, s[0:1]
	v_exp_f32_e32 v36, v65
	v_exp_f32_e32 v41, v49
	v_mul_f32_e32 v39, v40, v179
	global_store_dword v37, v39, s[0:1] offset:128
	v_mul_f32_e32 v37, v36, v178
	v_or_b32_e32 v39, 0x12000, v130
	global_store_dword v39, v37, s[0:1]
	v_exp_f32_e32 v37, v66
	v_mul_f32_e32 v42, v41, v178
	global_store_dword v39, v42, s[0:1] offset:128
	v_exp_f32_e32 v39, v50
	v_mul_f32_e32 v42, v37, v177
	v_or_b32_e32 v43, 0x14000, v130
	global_store_dword v43, v42, s[0:1]
	v_exp_f32_e32 v42, v67
	v_mul_f32_e32 v44, v39, v177
	global_store_dword v43, v44, s[0:1] offset:128
	v_exp_f32_e32 v43, v51
	v_cvt_pk_f16_f32 v37, v37, v42
	v_cvt_pk_f16_f32 v36, v38, v36
	v_cvt_pk_f16_f32 v38, v40, v41
	v_cvt_pk_f16_f32 v39, v39, v43
	ds_write2_b64 v187, v[32:33], v[36:37] offset1:2
	v_exp_f32_e32 v32, v68
	v_add_u32_e32 v40, 0x800, v187
	ds_write2_b64 v40, v[34:35], v[38:39] offset0:32 offset1:34
	v_exp_f32_e32 v34, v52
	v_exp_f32_e32 v36, v69
	v_exp_f32_e32 v37, v53
	v_mul_f32_e32 v33, v32, v175
	v_or_b32_e32 v35, 0x20000, v130
	global_store_dword v35, v33, s[0:1]
	v_mul_f32_e32 v33, v34, v175
	global_store_dword v35, v33, s[0:1] offset:128
	v_mul_f32_e32 v33, v36, v174
	v_or_b32_e32 v35, 0x22000, v130
	global_store_dword v35, v33, s[0:1]
	v_exp_f32_e32 v33, v70
	v_mul_f32_e32 v38, v37, v174
	global_store_dword v35, v38, s[0:1] offset:128
	v_exp_f32_e32 v35, v54
	v_mul_f32_e32 v38, v33, v173
	v_or_b32_e32 v39, 0x24000, v130
	global_store_dword v39, v38, s[0:1]
	v_exp_f32_e32 v38, v71
	v_mul_f32_e32 v41, v35, v173
	global_store_dword v39, v41, s[0:1] offset:128
	v_exp_f32_e32 v39, v55
	v_mul_f32_e32 v44, v42, v176
	v_mul_f32_e32 v41, v38, v172
	v_or_b32_e32 v42, 0x26000, v130
	v_cvt_pk_f16_f32 v32, v32, v36
	v_exp_f32_e32 v36, v72
	global_store_dword v42, v41, s[0:1]
	v_mul_f32_e32 v41, v39, v172
	v_cvt_pk_f16_f32 v33, v33, v38
	v_exp_f32_e32 v38, v56
	global_store_dword v42, v41, s[0:1] offset:128
	v_exp_f32_e32 v41, v73
	v_exp_f32_e32 v42, v57
	v_cvt_pk_f16_f32 v35, v35, v39
	v_cvt_pk_f16_f32 v34, v34, v37
	v_mul_f32_e32 v37, v36, v171
	v_or_b32_e32 v39, 0x30000, v130
	global_store_dword v39, v37, s[0:1]
	v_mul_f32_e32 v37, v38, v171
	v_or_b32_e32 v45, 0x16000, v130
	global_store_dword v39, v37, s[0:1] offset:128
	v_mul_f32_e32 v37, v41, v170
	v_or_b32_e32 v39, 0x32000, v130
	global_store_dword v45, v44, s[0:1]
	v_mul_f32_e32 v44, v43, v176
	global_store_dword v39, v37, s[0:1]
	v_exp_f32_e32 v37, v74
	v_mul_f32_e32 v43, v42, v170
	global_store_dword v39, v43, s[0:1] offset:128
	v_exp_f32_e32 v39, v58
	global_store_dword v45, v44, s[0:1] offset:128
	v_mul_f32_e32 v43, v37, v169
	v_or_b32_e32 v44, 0x34000, v130
	global_store_dword v44, v43, s[0:1]
	v_exp_f32_e32 v43, v75
	v_mul_f32_e32 v45, v39, v169
	global_store_dword v44, v45, s[0:1] offset:128
	v_exp_f32_e32 v44, v59
	v_mul_f32_e32 v45, v43, v168
	v_or_b32_e32 v46, 0x36000, v130
	global_store_dword v46, v45, s[0:1]
	v_mul_f32_e32 v45, v44, v168
	v_cvt_pk_f16_f32 v37, v37, v43
	v_cvt_pk_f16_f32 v36, v36, v41
	global_store_dword v46, v45, s[0:1] offset:128
	v_cvt_pk_f16_f32 v39, v39, v44
	v_cvt_pk_f16_f32 v38, v38, v42
	ds_write2_b64 v187, v[32:33], v[36:37] offset0:4 offset1:6
	ds_write2_b64 v40, v[34:35], v[38:39] offset0:36 offset1:38
	s_setprio 0
	ds_read_b64_tr_b16 v[32:33], v186
	ds_read_b64_tr_b16 v[34:35], v186 offset:288
	ds_read_b64_tr_b16 v[36:37], v185 offset:12288
	ds_read_b64_tr_b16 v[38:39], v185 offset:13056
	ds_read_b64_tr_b16 v[42:43], v185 offset:13120
	ds_read_b64_tr_b16 v[40:41], v185 offset:12352
	ds_read_b64_tr_b16 v[44:45], v186 offset:1152
	ds_read_b64_tr_b16 v[46:47], v186 offset:1440
	s_waitcnt lgkmcnt(4)
	v_mfma_f32_32x32x16_f16 v[0:15], v[32:35], v[36:39], v[0:15]
	s_waitcnt lgkmcnt(2)
	v_mfma_f32_32x32x16_f16 v[16:31], v[32:35], v[40:43], v[16:31]
	ds_read_b64_tr_b16 v[32:33], v185 offset:15360
	ds_read_b64_tr_b16 v[34:35], v185 offset:16128
	ds_read_b64_tr_b16 v[38:39], v185 offset:16192
	ds_read_b64_tr_b16 v[36:37], v185 offset:15424
	s_waitcnt lgkmcnt(2)
	v_mfma_f32_32x32x16_f16 v[0:15], v[44:47], v[32:35], v[0:15]
	s_waitcnt lgkmcnt(0)
	v_mfma_f32_32x32x16_f16 v[16:31], v[44:47], v[36:39], v[16:31]
	ds_read_b64_tr_b16 v[32:33], v186 offset:2304
	ds_read_b64_tr_b16 v[34:35], v186 offset:2592
	ds_read_b64_tr_b16 v[36:37], v185 offset:18432
	ds_read_b64_tr_b16 v[38:39], v185 offset:19200
	ds_read_b64_tr_b16 v[42:43], v185 offset:19264
	ds_read_b64_tr_b16 v[40:41], v185 offset:18496
	ds_read_b64_tr_b16 v[44:45], v186 offset:3456
	ds_read_b64_tr_b16 v[46:47], v186 offset:3744
	s_waitcnt lgkmcnt(4)
	v_mfma_f32_32x32x16_f16 v[0:15], v[32:35], v[36:39], v[0:15]
	s_waitcnt lgkmcnt(2)
	v_mfma_f32_32x32x16_f16 v[16:31], v[32:35], v[40:43], v[16:31]
	ds_read_b64_tr_b16 v[32:33], v185 offset:21504
	ds_read_b64_tr_b16 v[34:35], v185 offset:22272
	ds_read_b64_tr_b16 v[38:39], v185 offset:22336
	ds_read_b64_tr_b16 v[36:37], v185 offset:21568
	s_waitcnt lgkmcnt(2)
	v_mfma_f32_32x32x16_f16 v[0:15], v[44:47], v[32:35], v[0:15]
	s_waitcnt lgkmcnt(0)
	v_mfma_f32_32x32x16_f16 v[16:31], v[44:47], v[36:39], v[16:31]
	s_lshl_b32 s0, s2, 3
	s_and_b32 s0, s0, 0x7ffff800
	s_add_i32 s3, s3, s0
	s_lshl_b32 s0, s12, 7
	s_and_b32 s0, s0, 0x780
	s_add_u32 s0, s6, s0
	v_mov_b32_e32 v35, 0
	v_or_b32_e32 v32, s3, v184
	s_addc_u32 s1, s7, 0
	v_lshlrev_b32_e32 v34, 1, v164
	v_mov_b32_e32 v33, v35
	v_lshl_add_u64 v[36:37], s[0:1], 0, v[34:35]
	v_lshlrev_b64 v[38:39], 11, v[32:33]
	v_fma_mixlo_f16 v0, v0, v183, 0
	v_lshl_add_u64 v[38:39], v[36:37], 0, v[38:39]
	s_waitcnt vmcnt(63) expcnt(7) lgkmcnt(15)
	s_barrier
	global_store_short v[38:39], v0, off
	v_fma_mixlo_f16 v0, v16, v183, 0
	v_or_b32_e32 v34, 1, v32
	global_store_short v[38:39], v0, off offset:64
	v_lshlrev_b64 v[38:39], 11, v[34:35]
	v_fma_mixlo_f16 v16, v1, v182, 0
	v_lshl_add_u64 v[0:1], v[36:37], 0, v[38:39]
	global_store_short v[0:1], v16, off
	v_fma_mixlo_f16 v16, v17, v182, 0
	v_or_b32_e32 v34, 2, v32
	global_store_short v[0:1], v16, off offset:64
	v_lshlrev_b64 v[0:1], 11, v[34:35]
	v_fma_mixlo_f16 v2, v2, v181, 0
	v_lshl_add_u64 v[0:1], v[36:37], 0, v[0:1]
	global_store_short v[0:1], v2, off
	v_fma_mixlo_f16 v2, v18, v181, 0
	v_or_b32_e32 v34, 3, v32
	global_store_short v[0:1], v2, off offset:64
	v_lshlrev_b64 v[0:1], 11, v[34:35]
	v_fma_mixlo_f16 v2, v3, v180, 0
	v_lshl_add_u64 v[0:1], v[36:37], 0, v[0:1]
	global_store_short v[0:1], v2, off
	v_fma_mixlo_f16 v2, v19, v180, 0
	v_or_b32_e32 v34, 8, v32
	global_store_short v[0:1], v2, off offset:64
	v_lshlrev_b64 v[0:1], 11, v[34:35]
	v_fma_mixlo_f16 v2, v4, v179, 0
	v_lshl_add_u64 v[0:1], v[36:37], 0, v[0:1]
	global_store_short v[0:1], v2, off
	v_fma_mixlo_f16 v2, v20, v179, 0
	v_or_b32_e32 v34, 9, v32
	global_store_short v[0:1], v2, off offset:64
	v_lshlrev_b64 v[0:1], 11, v[34:35]
	v_fma_mixlo_f16 v2, v5, v178, 0
	v_lshl_add_u64 v[0:1], v[36:37], 0, v[0:1]
	global_store_short v[0:1], v2, off
	v_fma_mixlo_f16 v2, v21, v178, 0
	v_or_b32_e32 v34, 10, v32
	global_store_short v[0:1], v2, off offset:64
	v_lshlrev_b64 v[0:1], 11, v[34:35]
	v_fma_mixlo_f16 v2, v6, v177, 0
	v_lshl_add_u64 v[0:1], v[36:37], 0, v[0:1]
	global_store_short v[0:1], v2, off
	v_fma_mixlo_f16 v2, v22, v177, 0
	v_or_b32_e32 v34, 11, v32
	global_store_short v[0:1], v2, off offset:64
	v_lshlrev_b64 v[0:1], 11, v[34:35]
	v_fma_mixlo_f16 v2, v7, v176, 0
	v_lshl_add_u64 v[0:1], v[36:37], 0, v[0:1]
	global_store_short v[0:1], v2, off
	v_fma_mixlo_f16 v2, v23, v176, 0
	v_or_b32_e32 v34, 16, v32
	global_store_short v[0:1], v2, off offset:64
	v_lshlrev_b64 v[0:1], 11, v[34:35]
	v_fma_mixlo_f16 v2, v8, v175, 0
	v_lshl_add_u64 v[0:1], v[36:37], 0, v[0:1]
	global_store_short v[0:1], v2, off
	v_fma_mixlo_f16 v2, v24, v175, 0
	v_or_b32_e32 v34, 17, v32
	global_store_short v[0:1], v2, off offset:64
	v_lshlrev_b64 v[0:1], 11, v[34:35]
	v_fma_mixlo_f16 v2, v9, v174, 0
	v_lshl_add_u64 v[0:1], v[36:37], 0, v[0:1]
	global_store_short v[0:1], v2, off
	v_fma_mixlo_f16 v2, v25, v174, 0
	v_or_b32_e32 v34, 18, v32
	global_store_short v[0:1], v2, off offset:64
	v_lshlrev_b64 v[0:1], 11, v[34:35]
	v_fma_mixlo_f16 v2, v10, v173, 0
	v_lshl_add_u64 v[0:1], v[36:37], 0, v[0:1]
	global_store_short v[0:1], v2, off
	v_fma_mixlo_f16 v2, v26, v173, 0
	v_or_b32_e32 v34, 19, v32
	global_store_short v[0:1], v2, off offset:64
	v_lshlrev_b64 v[0:1], 11, v[34:35]
	v_fma_mixlo_f16 v2, v11, v172, 0
	v_lshl_add_u64 v[0:1], v[36:37], 0, v[0:1]
	global_store_short v[0:1], v2, off
	v_fma_mixlo_f16 v2, v27, v172, 0
	v_or_b32_e32 v34, 24, v32
	global_store_short v[0:1], v2, off offset:64
	v_lshlrev_b64 v[0:1], 11, v[34:35]
	v_fma_mixlo_f16 v2, v12, v171, 0
	v_lshl_add_u64 v[0:1], v[36:37], 0, v[0:1]
	global_store_short v[0:1], v2, off
	v_fma_mixlo_f16 v2, v28, v171, 0
	v_or_b32_e32 v34, 25, v32
	global_store_short v[0:1], v2, off offset:64
	v_lshlrev_b64 v[0:1], 11, v[34:35]
	v_fma_mixlo_f16 v2, v13, v170, 0
	v_lshl_add_u64 v[0:1], v[36:37], 0, v[0:1]
	global_store_short v[0:1], v2, off
	v_fma_mixlo_f16 v2, v29, v170, 0
	v_or_b32_e32 v34, 26, v32
	global_store_short v[0:1], v2, off offset:64
	v_lshlrev_b64 v[0:1], 11, v[34:35]
	v_fma_mixlo_f16 v2, v14, v169, 0
	v_lshl_add_u64 v[0:1], v[36:37], 0, v[0:1]
	global_store_short v[0:1], v2, off
	v_fma_mixlo_f16 v2, v30, v169, 0
	v_or_b32_e32 v34, 27, v32
	global_store_short v[0:1], v2, off offset:64
	v_lshlrev_b64 v[0:1], 11, v[34:35]
	v_fma_mixlo_f16 v2, v15, v168, 0
	v_lshl_add_u64 v[0:1], v[36:37], 0, v[0:1]
	global_store_short v[0:1], v2, off
	v_fma_mixlo_f16 v2, v31, v168, 0
	global_store_short v[0:1], v2, off offset:64
	s_endpgm
	.p2alignl 8, 3212836864

	.amdhsa_kernel _Z11attn_kernelILi0EEvPKDF16_S1_S1_PKfS3_PfPDF16_
		.amdhsa_group_segment_fixed_size 61440
		.amdhsa_private_segment_fixed_size 0
		.amdhsa_kernarg_size 56
		.amdhsa_user_sgpr_count 2
		.amdhsa_user_sgpr_dispatch_ptr 0
		.amdhsa_user_sgpr_queue_ptr 0
		.amdhsa_user_sgpr_kernarg_segment_ptr 1
		.amdhsa_user_sgpr_dispatch_id 0
		.amdhsa_user_sgpr_kernarg_preload_length 0
		.amdhsa_user_sgpr_kernarg_preload_offset 0
		.amdhsa_user_sgpr_private_segment_size 0
		.amdhsa_uses_dynamic_stack 0
		.amdhsa_enable_private_segment 0
		.amdhsa_system_sgpr_workgroup_id_x 1
		.amdhsa_system_sgpr_workgroup_id_y 0
		.amdhsa_system_sgpr_workgroup_id_z 0
		.amdhsa_system_sgpr_workgroup_info 0
		.amdhsa_system_vgpr_workitem_id 0
		.amdhsa_next_free_vgpr 244
		.amdhsa_next_free_sgpr 96
		.amdhsa_accum_offset 244
		.amdhsa_reserve_vcc 1
		.amdhsa_float_round_mode_32 0
		.amdhsa_float_round_mode_16_64 0
		.amdhsa_float_denorm_mode_32 3
		.amdhsa_float_denorm_mode_16_64 3
		.amdhsa_dx10_clamp 1
		.amdhsa_ieee_mode 1
		.amdhsa_fp16_overflow 0
		.amdhsa_tg_split 0
		.amdhsa_exception_fp_ieee_invalid_op 0
		.amdhsa_exception_fp_denorm_src 0
		.amdhsa_exception_fp_ieee_div_zero 0
		.amdhsa_exception_fp_ieee_overflow 0
		.amdhsa_exception_fp_ieee_underflow 0
		.amdhsa_exception_fp_ieee_inexact 0
		.amdhsa_exception_int_div_zero 0
	.end_amdhsa_kernel

amdhsa.kernels:
  - .agpr_count:     0
    .args:
      - .actual_access:  read_only
        .address_space:  global
        .offset:         0
        .size:           8
        .value_kind:     global_buffer
      - .actual_access:  read_only
        .address_space:  global
        .offset:         8
        .size:           8
        .value_kind:     global_buffer
      - .actual_access:  read_only
        .address_space:  global
        .offset:         16
        .size:           8
        .value_kind:     global_buffer
      - .actual_access:  read_only
        .address_space:  global
        .offset:         24
        .size:           8
        .value_kind:     global_buffer
      - .actual_access:  read_only
        .address_space:  global
        .offset:         32
        .size:           8
        .value_kind:     global_buffer
      - .actual_access:  write_only
        .address_space:  global
        .offset:         40
        .size:           8
        .value_kind:     global_buffer
      - .actual_access:  write_only
        .address_space:  global
        .offset:         48
        .size:           8
        .value_kind:     global_buffer
    .group_segment_fixed_size: 0
    .kernarg_segment_align: 8
    .kernarg_segment_size: 56
    .language:       OpenCL C
    .language_version:
      - 2
      - 0
    .max_flat_workgroup_size: 256
    .name:           _Z10cvt_kernelPKfS0_S0_S0_S0_PDF16_S1_
    .private_segment_fixed_size: 0
    .sgpr_count:     22
    .sgpr_spill_count: 0
    .symbol:         _Z10cvt_kernelPKfS0_S0_S0_S0_PDF16_S1_.kd
    .uniform_work_group_size: 1
    .uses_dynamic_stack: false
    .vgpr_count:     14
    .vgpr_spill_count: 0
    .wavefront_size: 64
  - .agpr_count:     0
    .args:
      - .actual_access:  read_only
        .address_space:  global
        .offset:         0
        .size:           8
        .value_kind:     global_buffer
      - .actual_access:  read_only
        .address_space:  global
        .offset:         8
        .size:           8
        .value_kind:     global_buffer
      - .actual_access:  write_only
        .address_space:  global
        .offset:         16
        .size:           8
        .value_kind:     global_buffer
      - .actual_access:  write_only
        .address_space:  global
        .offset:         24
        .size:           8
        .value_kind:     global_buffer
    .group_segment_fixed_size: 18432
    .kernarg_segment_align: 8
    .kernarg_segment_size: 32
    .language:       OpenCL C
    .language_version:
      - 2
      - 0
    .max_flat_workgroup_size: 256
    .name:           _Z12stats_kernelPKDF16_S0_PfS1_
    .private_segment_fixed_size: 0
    .sgpr_count:     19
    .sgpr_spill_count: 0
    .symbol:         _Z12stats_kernelPKDF16_S0_PfS1_.kd
    .uniform_work_group_size: 1
    .uses_dynamic_stack: false
    .vgpr_count:     100
    .vgpr_spill_count: 0
    .wavefront_size: 64
  - .agpr_count:     0
    .args:
      - .actual_access:  read_only
        .address_space:  global
        .offset:         0
        .size:           8
        .value_kind:     global_buffer
      - .actual_access:  read_only
        .address_space:  global
        .offset:         8
        .size:           8
        .value_kind:     global_buffer
      - .actual_access:  read_only
        .address_space:  global
        .offset:         16
        .size:           8
        .value_kind:     global_buffer
      - .actual_access:  read_only
        .address_space:  global
        .offset:         24
        .size:           8
        .value_kind:     global_buffer
      - .actual_access:  write_only
        .address_space:  global
        .offset:         32
        .size:           8
        .value_kind:     global_buffer
      - .actual_access:  write_only
        .address_space:  global
        .offset:         40
        .size:           8
        .value_kind:     global_buffer
      - .actual_access:  write_only
        .address_space:  global
        .offset:         48
        .size:           8
        .value_kind:     global_buffer
      - .actual_access:  read_only
        .address_space:  global
        .offset:         56
        .size:           8
        .value_kind:     global_buffer
      - .offset:         64
        .size:           4
        .value_kind:     by_value
    .group_segment_fixed_size: 0
    .kernarg_segment_align: 8
    .kernarg_segment_size: 68
    .language:       OpenCL C
    .language_version:
      - 2
      - 0
    .max_flat_workgroup_size: 512
    .name:           _Z11gemm_kernelILi256ELi192ELi4ELi2ELi0EEvPKDF16_S1_PKfS3_PDF16_S4_S4_Pfi
    .private_segment_fixed_size: 0
    .sgpr_count:     27
    .sgpr_spill_count: 0
    .symbol:         _Z11gemm_kernelILi256ELi192ELi4ELi2ELi0EEvPKDF16_S1_PKfS3_PDF16_S4_S4_Pfi.kd
    .uniform_work_group_size: 1
    .uses_dynamic_stack: false
    .vgpr_count:     249
    .vgpr_spill_count: 0
    .wavefront_size: 64
  - .agpr_count:     0
    .args:
      - .actual_access:  read_only
        .address_space:  global
        .offset:         0
        .size:           8
        .value_kind:     global_buffer
      - .actual_access:  read_only
        .address_space:  global
        .offset:         8
        .size:           8
        .value_kind:     global_buffer
      - .actual_access:  read_only
        .address_space:  global
        .offset:         16
        .size:           8
        .value_kind:     global_buffer
      - .actual_access:  read_only
        .address_space:  global
        .offset:         24
        .size:           8
        .value_kind:     global_buffer
      - .actual_access:  read_only
        .address_space:  global
        .offset:         32
        .size:           8
        .value_kind:     global_buffer
      - .actual_access:  read_only
        .address_space:  global
        .offset:         40
        .size:           8
        .value_kind:     global_buffer
      - .actual_access:  read_only
        .address_space:  global
        .offset:         48
        .size:           8
        .value_kind:     global_buffer
      - .actual_access:  write_only
        .address_space:  global
        .offset:         56
        .size:           8
        .value_kind:     global_buffer
      - .offset:         64
        .size:           4
        .value_kind:     by_value
    .group_segment_fixed_size: 0
    .kernarg_segment_align: 8
    .kernarg_segment_size: 68
    .language:       OpenCL C
    .language_version:
      - 2
      - 0
    .max_flat_workgroup_size: 512
    .name:           _Z11gemm_kernelILi128ELi128ELi4ELi2ELi1EEvPKDF16_S1_PKfS3_PDF16_S4_S4_Pfi
    .private_segment_fixed_size: 0
    .sgpr_count:     19
    .sgpr_spill_count: 0
    .symbol:         _Z11gemm_kernelILi128ELi128ELi4ELi2ELi1EEvPKDF16_S1_PKfS3_PDF16_S4_S4_Pfi.kd
    .uniform_work_group_size: 1
    .uses_dynamic_stack: false
    .vgpr_count:     88
    .vgpr_spill_count: 0
    .wavefront_size: 64
  - .agpr_count:     0
    .args:
      - .actual_access:  read_only
        .address_space:  global
        .offset:         0
        .size:           8
        .value_kind:     global_buffer
      - .actual_access:  read_only
        .address_space:  global
        .offset:         8
        .size:           8
        .value_kind:     global_buffer
      - .actual_access:  read_only
        .address_space:  global
        .offset:         16
        .size:           8
        .value_kind:     global_buffer
      - .actual_access:  read_only
        .address_space:  global
        .offset:         24
        .size:           8
        .value_kind:     global_buffer
      - .actual_access:  read_only
        .address_space:  global
        .offset:         32
        .size:           8
        .value_kind:     global_buffer
      - .actual_access:  write_only
        .address_space:  global
        .offset:         40
        .size:           8
        .value_kind:     global_buffer
      - .actual_access:  write_only
        .address_space:  global
        .offset:         48
        .size:           8
        .value_kind:     global_buffer
    .group_segment_fixed_size: 61440
    .kernarg_segment_align: 8
    .kernarg_segment_size: 56
    .language:       OpenCL C
    .language_version:
      - 2
      - 0
    .max_flat_workgroup_size: 256
    .name:           _Z11attn_kernelILi0EEvPKDF16_S1_S1_PKfS3_PfPDF16_
    .private_segment_fixed_size: 0
    .sgpr_count:     30
    .sgpr_spill_count: 0
    .symbol:         _Z11attn_kernelILi0EEvPKDF16_S1_S1_PKfS3_PfPDF16_.kd
    .uniform_work_group_size: 1
    .uses_dynamic_stack: false
    .vgpr_count:     244
    .vgpr_spill_count: 0
    .wavefront_size: 64
